# speedup vs baseline: 1.0105x; 1.0105x over previous
.LBB5_99:
	s_or_b64 exec, exec, s[18:19]
	s_waitcnt lgkmcnt(0)
	s_barrier
	v_or_b32_e32 v1, s45, v128
	v_cmp_eq_u32_e64 s[8:9], 0, v1
	s_and_saveexec_b64 s[16:17], s[8:9]
	s_cbranch_execz .LBB5_101
	v_mov_b32_e32 v61, 0x23e40
	ds_read_b128 v[42:45], v61
	ds_read_b128 v[46:49], v61 offset:16
	ds_read_b128 v[50:53], v61 offset:32
	ds_read_b128 v[54:57], v61 offset:48
	ds_read_b128 v[58:61], v61 offset:64
	s_lshl_b32 s18, s33, 8
	s_add_u32 s28, s34, s18
	s_addc_u32 s29, s35, 0
	s_ashr_i32 s37, s36, 31
	s_lshl_b64 s[18:19], s[36:37], 3
	s_add_u32 s18, s28, s18
	s_addc_u32 s19, s29, s19
	s_waitcnt lgkmcnt(4)
	v_add_f32_e32 v42, 0, v42
	v_add_f32_e32 v43, 0, v43
	v_add_f32_e32 v42, v42, v44
	v_add_f32_e32 v43, v43, v45
	s_waitcnt lgkmcnt(3)
	v_add_f32_e32 v42, v42, v46
	v_add_f32_e32 v43, v43, v47
	v_add_f32_e32 v42, v42, v48
	v_add_f32_e32 v43, v43, v49
	s_waitcnt lgkmcnt(2)
	v_add_f32_e32 v42, v42, v50
	v_add_f32_e32 v43, v43, v51
	v_add_f32_e32 v42, v42, v52
	v_add_f32_e32 v43, v43, v53
	s_waitcnt lgkmcnt(1)
	v_add_f32_e32 v42, v42, v54
	v_add_f32_e32 v43, v43, v55
	v_add_f32_e32 v42, v42, v56
	v_add_f32_e32 v43, v43, v57
	s_waitcnt lgkmcnt(0)
	v_add_f32_e32 v42, v42, v58
	v_add_f32_e32 v43, v43, v59
	v_add_f32_e32 v42, v42, v60
	v_add_f32_e32 v43, v43, v61
	v_or_b32_e32 v43, 1, v43
	v_mov_b32_e32 v61, 0x150000
	global_store_dwordx2 v61, v[42:43], s[18:19] offset:2048 sc1

.LBB5_141:
	s_or_b64 exec, exec, s[24:25]
	s_waitcnt lgkmcnt(0)
	s_barrier
	s_and_saveexec_b64 s[12:13], s[8:9]
	s_cbranch_execz .LBB5_143
	v_mov_b32_e32 v73, 0x23e40
	ds_read_b128 v[54:57], v73
	ds_read_b128 v[58:61], v73 offset:16
	ds_read_b128 v[62:65], v73 offset:32
	ds_read_b128 v[66:69], v73 offset:48
	ds_read_b128 v[70:73], v73 offset:64
	s_lshl_b32 s18, s33, 8
	s_add_u32 s24, s34, s18
	s_addc_u32 s25, s35, 0
	s_ashr_i32 s37, s36, 31
	s_lshl_b64 s[18:19], s[36:37], 3
	s_add_u32 s18, s24, s18
	s_addc_u32 s19, s25, s19
	s_waitcnt lgkmcnt(4)
	v_add_f32_e32 v54, 0, v54
	v_add_f32_e32 v55, 0, v55
	v_add_f32_e32 v54, v54, v56
	v_add_f32_e32 v55, v55, v57
	s_waitcnt lgkmcnt(3)
	v_add_f32_e32 v54, v54, v58
	v_add_f32_e32 v55, v55, v59
	v_add_f32_e32 v54, v54, v60
	v_add_f32_e32 v55, v55, v61
	s_waitcnt lgkmcnt(2)
	v_add_f32_e32 v54, v54, v62
	v_add_f32_e32 v55, v55, v63
	v_add_f32_e32 v54, v54, v64
	v_add_f32_e32 v55, v55, v65
	s_waitcnt lgkmcnt(1)
	v_add_f32_e32 v54, v54, v66
	v_add_f32_e32 v55, v55, v67
	v_add_f32_e32 v54, v54, v68
	v_add_f32_e32 v55, v55, v69
	s_waitcnt lgkmcnt(0)
	v_add_f32_e32 v54, v54, v70
	v_add_f32_e32 v55, v55, v71
	v_add_f32_e32 v54, v54, v72
	v_add_f32_e32 v55, v55, v73
	v_or_b32_e32 v55, 1, v55
	v_mov_b32_e32 v73, 0x151000
	global_store_dwordx2 v73, v[54:55], s[18:19] sc1

.LBB5_177:
	s_or_b64 exec, exec, s[14:15]
	s_waitcnt lgkmcnt(0)
	s_barrier
	s_and_saveexec_b64 s[10:11], s[8:9]
	s_cbranch_execz .LBB5_179
	v_mov_b32_e32 v43, 0x23e40
	ds_read_b128 v[24:27], v43
	ds_read_b128 v[28:31], v43 offset:16
	ds_read_b128 v[32:35], v43 offset:32
	ds_read_b128 v[36:39], v43 offset:48
	ds_read_b128 v[40:43], v43 offset:64
	s_waitcnt vmcnt(8)
	s_lshl_b32 s8, s33, 8
	s_add_u32 s12, s34, s8
	s_addc_u32 s13, s35, 0
	s_ashr_i32 s37, s36, 31
	s_lshl_b64 s[8:9], s[36:37], 3
	s_add_u32 s8, s12, s8
	s_addc_u32 s9, s13, s9
	s_waitcnt lgkmcnt(4)
	v_add_f32_e32 v24, 0, v24
	v_add_f32_e32 v25, 0, v25
	v_add_f32_e32 v24, v24, v26
	v_add_f32_e32 v25, v25, v27
	s_waitcnt lgkmcnt(3)
	v_add_f32_e32 v24, v24, v28
	v_add_f32_e32 v25, v25, v29
	v_add_f32_e32 v24, v24, v30
	v_add_f32_e32 v25, v25, v31
	s_waitcnt lgkmcnt(2)
	v_add_f32_e32 v24, v24, v32
	v_add_f32_e32 v25, v25, v33
	v_add_f32_e32 v24, v24, v34
	v_add_f32_e32 v25, v25, v35
	s_waitcnt lgkmcnt(1)
	v_add_f32_e32 v24, v24, v36
	v_add_f32_e32 v25, v25, v37
	v_add_f32_e32 v24, v24, v38
	v_add_f32_e32 v25, v25, v39
	s_waitcnt lgkmcnt(0)
	v_add_f32_e32 v24, v24, v40
	v_add_f32_e32 v25, v25, v41
	v_add_f32_e32 v24, v24, v42
	v_add_f32_e32 v25, v25, v43
	v_or_b32_e32 v25, 1, v25
	v_mov_b32_e32 v43, 0x151000
	global_store_dwordx2 v43, v[24:25], s[8:9] offset:2048 sc1
